# next-block prefetch: at the attention unit epilogue one dword per Q row line of the NEXT unit is touched so the next prologue's Q loads hit L2; on top of v9_prohoist
# speedup vs baseline: 1.0020x; 1.0020x over previous
.LBB0_1109:
	s_setprio 0
	v_readlane_b32 s0, v254, 4
	v_readlane_b32 s1, v254, 5
	s_load_dword s2, s[0:1], 0x0
	s_waitcnt lgkmcnt(0)
	s_add_i32 s2, s2, s15
	s_cmpk_gt_u32 s2, 0x7ff
	s_cbranch_scc1 .Latt_qt_skip
	s_lshr_b32 s3, s2, 8
	s_mulk_i32 s3, 0x2100
	s_bfe_u32 s7, s2, 0x50003
	s_lshl_b32 s7, s7, 8
	s_add_i32 s3, s3, s7
	s_addk_i32 s3, 0x100
	s_and_b32 s2, s2, 7
	s_mul_i32 s2, s2, 0xc0
	v_add_u32_e32 v236, s3, v214
	v_mul_u32_u24_e32 v236, 0x600, v236
	v_mbcnt_lo_u32_b32 v237, -1, 0
	v_mbcnt_hi_u32_b32 v237, -1, v237
	v_and_b32_e32 v237, 32, v237
	v_lshlrev_b32_e32 v237, 2, v237
	v_add3_u32 v236, v236, v237, s2
	global_load_dword v237, v236, s[46:47]
.Latt_qt_skip:
	s_nop 1
	v_mov_b32_e32 v4, v224
	s_nop 1
	v_permlane32_swap_b32_e32 v224, v4
	v_add_f32_e32 v4, v224, v4
	v_div_scale_f32 v5, s[0:1], v4, v4, 1.0
	v_rcp_f32_e32 v6, v5
	s_lshl_b32 s30, s35, 7
	v_mov_b32_e32 v199, v3
	s_mov_b64 s[0:1], 0x1701b400
	v_fma_f32 v7, -v5, v6, 1.0
	v_fmac_f32_e32 v6, v7, v6
	v_div_scale_f32 v7, vcc, 1.0, v4, 1.0
	v_mul_f32_e32 v8, v7, v6
	v_fma_f32 v9, -v5, v8, v7
	v_fmac_f32_e32 v8, v9, v6
	v_fma_f32 v5, -v5, v8, v7
	v_div_fmas_f32 v5, v5, v6, v8
	v_lshlrev_b64 v[6:7], 11, v[200:201]
	v_lshl_add_u64 v[6:7], s[44:45], 0, v[6:7]
	v_lshl_add_u64 v[6:7], v[6:7], 0, s[30:31]
	v_lshl_add_u64 v[6:7], v[6:7], 0, v[198:199]
	v_div_fixup_f32 v4, v5, v4, 1.0
	v_lshl_add_u64 v[8:9], v[6:7], 0, s[0:1]
	v_mbcnt_lo_u32_b32 v6, -1, 0
	v_mbcnt_hi_u32_b32 v6, -1, v6
	v_and_b32_e32 v6, 32, v6
	v_lshrrev_b32_e32 v6, 2, v6
	v_mov_b32_e32 v7, 0
	v_lshl_add_u64 v[8:9], v[8:9], 0, v[6:7]
	v_pk_mul_f32 v[10:11], v[36:37], v[4:5] op_sel_hi:[1,0]
	v_pk_mul_f32 v[12:13], v[38:39], v[4:5] op_sel_hi:[1,0]
	v_pk_mul_f32 v[14:15], v[40:41], v[4:5] op_sel_hi:[1,0]
	v_pk_mul_f32 v[16:17], v[42:43], v[4:5] op_sel_hi:[1,0]
	v_cvt_pk_bf16_f32 v20, v10, v11
	v_cvt_pk_bf16_f32 v21, v12, v13
	v_cvt_pk_bf16_f32 v22, v14, v15
	v_cvt_pk_bf16_f32 v23, v16, v17
	s_nop 1
	v_permlane32_swap_b32_e32 v20, v22
	v_permlane32_swap_b32_e32 v21, v23
	global_store_dwordx4 v[8:9], v[20:23], off
	v_pk_mul_f32 v[10:11], v[44:45], v[4:5] op_sel_hi:[1,0]
	v_pk_mul_f32 v[12:13], v[46:47], v[4:5] op_sel_hi:[1,0]
	v_pk_mul_f32 v[14:15], v[48:49], v[4:5] op_sel_hi:[1,0]
	v_pk_mul_f32 v[16:17], v[50:51], v[4:5] op_sel_hi:[1,0]
	v_cvt_pk_bf16_f32 v24, v10, v11
	v_cvt_pk_bf16_f32 v25, v12, v13
	v_cvt_pk_bf16_f32 v26, v14, v15
	v_cvt_pk_bf16_f32 v27, v16, v17
	s_nop 1
	v_permlane32_swap_b32_e32 v24, v26
	v_permlane32_swap_b32_e32 v25, v27
	global_store_dwordx4 v[8:9], v[24:27], off offset:32
	v_pk_mul_f32 v[10:11], v[52:53], v[4:5] op_sel_hi:[1,0]
	v_pk_mul_f32 v[12:13], v[54:55], v[4:5] op_sel_hi:[1,0]
	v_pk_mul_f32 v[14:15], v[56:57], v[4:5] op_sel_hi:[1,0]
	v_pk_mul_f32 v[16:17], v[58:59], v[4:5] op_sel_hi:[1,0]
	v_cvt_pk_bf16_f32 v28, v10, v11
	v_cvt_pk_bf16_f32 v29, v12, v13
	v_cvt_pk_bf16_f32 v30, v14, v15
	v_cvt_pk_bf16_f32 v31, v16, v17
	s_nop 1
	v_permlane32_swap_b32_e32 v28, v30
	v_permlane32_swap_b32_e32 v29, v31
	global_store_dwordx4 v[8:9], v[28:31], off offset:64
	v_pk_mul_f32 v[10:11], v[60:61], v[4:5] op_sel_hi:[1,0]
	v_pk_mul_f32 v[12:13], v[62:63], v[4:5] op_sel_hi:[1,0]
	v_pk_mul_f32 v[14:15], v[64:65], v[4:5] op_sel_hi:[1,0]
	v_pk_mul_f32 v[16:17], v[66:67], v[4:5] op_sel_hi:[1,0]
	v_cvt_pk_bf16_f32 v32, v10, v11
	v_cvt_pk_bf16_f32 v33, v12, v13
	v_cvt_pk_bf16_f32 v34, v14, v15
	v_cvt_pk_bf16_f32 v35, v16, v17
	s_nop 1
	v_permlane32_swap_b32_e32 v32, v34
	v_permlane32_swap_b32_e32 v33, v35
	global_store_dwordx4 v[8:9], v[32:35], off offset:96
	v_readlane_b32 s0, v254, 4
	v_readlane_b32 s1, v254, 5
	s_load_dword s0, s[0:1], 0x0
	s_waitcnt lgkmcnt(0)
	s_add_i32 s15, s0, s15
	s_cmp_lt_i32 s15, s14
	s_cbranch_scc0 .LBB0_1140
